# f1_fullline
# baseline (speedup 1.0000x reference)
.Lepi_d0:
	s_waitcnt vmcnt(0)
	s_lshl_b32 s35, s29, 11
	s_lshl_b32 s30, s5, 6
	s_sub_i32 s31, 0x80, s30
	s_sub_i32 s31, s31, s30
	v_mbcnt_lo_u32_b32 v104, -1, 0
	v_mbcnt_hi_u32_b32 v104, -1, v104
	v_lshrrev_b32_e32 v105, 3, v104
	v_and_b32_e32 v106, 7, v104
	v_mul_u32_u24_e32 v108, 0xd0, v105
	v_lshl_add_u32 v108, v106, 4, v108
	v_add_u32_e32 v108, s24, v108
	v_add_u32_e32 v108, s30, v108
	v_lshlrev_b32_e32 v109, 11, v105
	v_lshl_add_u32 v109, v106, 4, v109
	v_add_u32_e32 v102, s31, v102
	s_lshr_b32 s28, s30, 1
	s_add_i32 s28, s28, s34
	s_lshr_b32 s48, s28, 10
	s_and_b32 s28, s28, 0x3ff
	s_lshl_b32 s28, s28, 1
	s_cmp_eq_u32 s48, 1
	s_cselect_b64 s[44:45], s[16:17], s[14:15]
	s_cmp_eq_u32 s48, 2
	s_cselect_b64 s[44:45], s[18:19], s[44:45]
	s_add_u32 s44, s44, s28
	s_addc_u32 s45, s45, 0
	s_add_u32 s44, s44, s35
	s_addc_u32 s45, s45, 0
	s_lshr_b32 s28, s31, 1
	s_add_i32 s28, s28, s34
	s_lshr_b32 s48, s28, 10
	s_and_b32 s28, s28, 0x3ff
	s_lshl_b32 s28, s28, 1
	s_cmp_eq_u32 s48, 1
	s_cselect_b64 s[46:47], s[16:17], s[14:15]
	s_cmp_eq_u32 s48, 2
	s_cselect_b64 s[46:47], s[18:19], s[46:47]
	s_add_u32 s46, s46, s28
	s_addc_u32 s47, s47, 0
	s_add_u32 s46, s46, s35
	s_addc_u32 s47, s47, 0
	s_waitcnt lgkmcnt(0)
	ds_read_b128 v[2:5], v108 offset:0
	ds_read_b128 v[6:9], v108 offset:1664
	ds_read_b128 v[10:13], v108 offset:3328
	ds_read_b128 v[14:17], v108 offset:4992
	ds_read_b128 v[18:21], v108 offset:6656
	ds_read_b128 v[22:25], v108 offset:8320
	ds_read_b128 v[26:29], v108 offset:9984
	ds_read_b128 v[30:33], v108 offset:11648
	ds_read_b128 v[34:37], v102 offset:0
	ds_read_b128 v[38:41], v102 offset:3328
	ds_read_b128 v[42:45], v102 offset:6656
	ds_read_b128 v[46:49], v102 offset:9984
	v_add_u32_e32 v110, 16384, v109
	v_add_u32_e32 v111, 32768, v109
	v_add_u32_e32 v112, 49152, v109
	v_add_u32_e32 v113, 65536, v109
	v_add_u32_e32 v114, 81920, v109
	v_add_u32_e32 v115, 98304, v109
	v_add_u32_e32 v116, 114688, v109
	v_add_u32_e32 v117, 32768, v0
	v_add_u32_e32 v118, 65536, v0
	v_add_u32_e32 v119, 98304, v0
	s_waitcnt lgkmcnt(11)
	global_store_dwordx4 v109, v[2:5], s[44:45] sc1
	s_waitcnt lgkmcnt(10)
	global_store_dwordx4 v110, v[6:9], s[44:45] sc1
	s_waitcnt lgkmcnt(9)
	global_store_dwordx4 v111, v[10:13], s[44:45] sc1
	s_waitcnt lgkmcnt(8)
	global_store_dwordx4 v112, v[14:17], s[44:45] sc1
	s_waitcnt lgkmcnt(7)
	global_store_dwordx4 v113, v[18:21], s[44:45] sc1
	s_waitcnt lgkmcnt(6)
	global_store_dwordx4 v114, v[22:25], s[44:45] sc1
	s_waitcnt lgkmcnt(5)
	global_store_dwordx4 v115, v[26:29], s[44:45] sc1
	s_waitcnt lgkmcnt(4)
	global_store_dwordx4 v116, v[30:33], s[44:45] sc1
	s_waitcnt lgkmcnt(3)
	global_store_dwordx4 v0, v[34:37], s[46:47] sc1
	s_waitcnt lgkmcnt(2)
	global_store_dwordx4 v117, v[38:41], s[46:47] sc1
	s_waitcnt lgkmcnt(1)
	global_store_dwordx4 v118, v[42:45], s[46:47] sc1
	s_waitcnt lgkmcnt(0)
	global_store_dwordx4 v119, v[46:49], s[46:47] sc1
	s_branch .LBB2_2
